# barrier waits convert with waves 1-7; P11 flush: all waves finish their leftover batch, only waves 1-5 fetch new batches (P13 remap kept)
# baseline (speedup 1.0000x reference)
; #define BOTH(k) (IN(k) && IN((k) + 1))
; #define GRID_BAR_CV() xcd_barrier_cv(bar, cvw)
; __device__ __forceinline__ void xcd_barrier_cv(const XcdBarrier& b, const CvWork& w) {
;     asm volatile("s_waitcnt vmcnt(0)" ::: "memory");
;     const unsigned g0 = w.rel[0];
;     __syncthreads();
;     if (b.wave == 0) {
;         xb_wave0(b, w.rel + 1, g0 + 1u);
;         w.rel[0] = g0 + 1u;
;     } else if (b.wave != 0) {
;         unsigned guard = 0;
;         while (w.rel[0] == g0) { if (w.rel[1] == g0 + 1u || b.wave > 4) { __builtin_amdgcn_s_sleep(1); continue; }
;             if (!cv_one(w)) __builtin_amdgcn_s_sleep(4); if (++guard > (1u << 22)) break; }
; __global__ void __launch_bounds__(NTHR, 2) fwd(Args args) {
;     ...
;         if (BOTH(0)) GRID_BAR_CV();
.LBB0_193:
	s_add_i32 s0, 0, 0x20170
	s_waitcnt vmcnt(0)
	s_waitcnt vmcnt(16)
	v_mov_b32_e32 v0, s0
	ds_read_b32 v2, v0
	s_cmp_eq_u32 s89, 0
	s_waitcnt lgkmcnt(0)
	s_barrier
	s_cbranch_scc1 .LBB0_219
	v_mov_b32_e32 v0, s0
	ds_read_b32 v0, v0
	s_waitcnt lgkmcnt(0)
	v_cmp_ne_u32_e32 vcc, v0, v2
	s_cbranch_vccnz .LBB0_218
	s_cmp_gt_i32 s89, 7
	s_cselect_b64 s[0:1], -1, 0
	s_lshl_b32 s2, s89, 3
	s_add_i32 s3, 0, 0x20174
	s_add_i32 s10, s2, 0
	v_add_u32_e32 v3, 1, v2
	s_mov_b32 s28, 0
	s_waitcnt vmcnt(15)
	v_mov_b32_e32 v4, s3
	s_add_i32 s2, s10, 0x20180
	v_mov_b32_e32 v1, 0
	s_mov_b32 s3, 0x10000
	v_mov_b32_e32 v5, 0x10001
	s_add_i32 s10, s10, 0x20184
	s_movk_i32 s11, 0x4000
	s_mov_b32 s12, 0x8000
	s_mov_b32 s13, 0xc000
	s_mov_b32 s14, 0x14000
	s_mov_b32 s15, 0x18000
	s_mov_b32 s16, 0x1c000
	s_mov_b32 s17, 0x20000
	s_mov_b32 s18, 0x24000
	s_mov_b32 s19, 0x28000
	s_mov_b32 s20, 0x2c000
	s_mov_b32 s21, 0x30000
	s_mov_b32 s22, 0x34000
	s_mov_b32 s23, 0x38000
	s_mov_b32 s24, 0x3c000
	s_mov_b32 s25, 0xc3e00000
	s_movk_i32 s26, 0x1000
	s_add_i32 s27, 0, 0x20170
	v_mov_b32_e32 v6, 0x43e00000
	s_branch .LBB0_197

; #define BOTH(k) (IN(k) && IN((k) + 1))
; #define GRID_BAR_CV() xcd_barrier_cv(bar, cvw)
; __device__ __forceinline__ void xcd_barrier_cv(const XcdBarrier& b, const CvWork& w) {
;     asm volatile("s_waitcnt vmcnt(0)" ::: "memory");
;     const unsigned g0 = w.rel[0];
;     __syncthreads();
;     if (b.wave == 0) {
;         xb_wave0(b, w.rel + 1, g0 + 1u);
;         w.rel[0] = g0 + 1u;
;     } else if (b.wave != 0) {
;         unsigned guard = 0;
;         while (w.rel[0] == g0) { if (w.rel[1] == g0 + 1u || b.wave > 4) { __builtin_amdgcn_s_sleep(1); continue; }
;             if (!cv_one(w)) __builtin_amdgcn_s_sleep(4); if (++guard > (1u << 22)) break; }
; __global__ void __launch_bounds__(NTHR, 2) fwd(Args args) {
;     ...
;         if (BOTH(1)) GRID_BAR_CV();
.LBB0_359:
	s_cmp_lt_i32 s81, 3
	s_cbranch_scc1 .LBB0_431
	s_add_i32 s0, 0, 0x20170
	s_waitcnt vmcnt(0)
	v_mov_b32_e32 v0, s0
	ds_read_b32 v2, v0
	s_cmp_eq_u32 s89, 0
	s_waitcnt vmcnt(0) lgkmcnt(0)
	s_barrier
	s_cbranch_scc1 .LBB0_386
	v_mov_b32_e32 v0, s0
	ds_read_b32 v0, v0
	s_waitcnt lgkmcnt(0)
	v_cmp_ne_u32_e32 vcc, v0, v2
	s_cbranch_vccnz .LBB0_385
	s_cmp_gt_i32 s89, 7
	s_cselect_b64 s[0:1], -1, 0
	s_lshl_b32 s2, s89, 3
	s_add_i32 s3, 0, 0x20174
	s_add_i32 s10, s2, 0
	v_add_u32_e32 v3, 1, v2
	s_mov_b32 s28, 0
	v_mov_b32_e32 v4, s3
	s_add_i32 s2, s10, 0x20180
	v_mov_b32_e32 v1, 0
	s_mov_b32 s3, 0x10000
	v_mov_b32_e32 v5, 0x10001
	s_add_i32 s10, s10, 0x20184
	s_movk_i32 s11, 0x4000
	s_mov_b32 s12, 0x8000
	s_mov_b32 s13, 0xc000
	s_mov_b32 s14, 0x14000
	s_mov_b32 s15, 0x18000
	s_mov_b32 s16, 0x1c000
	s_mov_b32 s17, 0x20000
	s_mov_b32 s18, 0x24000
	s_mov_b32 s19, 0x28000
	s_mov_b32 s20, 0x2c000
	s_mov_b32 s21, 0x30000
	s_mov_b32 s22, 0x34000
	s_mov_b32 s23, 0x38000
	s_mov_b32 s24, 0x3c000
	s_mov_b32 s25, 0xc3e00000
	s_movk_i32 s26, 0x1000
	s_add_i32 s27, 0, 0x20170
	v_mov_b32_e32 v6, 0x43e00000
	s_branch .LBB0_364

; #define BOTH(k) (IN(k) && IN((k) + 1))
; #define GRID_BAR_CV() xcd_barrier_cv(bar, cvw)
; __device__ __forceinline__ void xcd_barrier_cv(const XcdBarrier& b, const CvWork& w) {
;     asm volatile("s_waitcnt vmcnt(0)" ::: "memory");
;     const unsigned g0 = w.rel[0];
;     __syncthreads();
;     if (b.wave == 0) {
;         xb_wave0(b, w.rel + 1, g0 + 1u);
;         w.rel[0] = g0 + 1u;
;     } else if (b.wave != 0) {
;         unsigned guard = 0;
;         while (w.rel[0] == g0) { if (w.rel[1] == g0 + 1u || b.wave > 4) { __builtin_amdgcn_s_sleep(1); continue; }
;             if (!cv_one(w)) __builtin_amdgcn_s_sleep(4); if (++guard > (1u << 22)) break; }
; __global__ void __launch_bounds__(NTHR, 2) fwd(Args args) {
;     ...
;         if (BOTH(2)) GRID_BAR_CV();
.LBB0_479:
	s_cmp_gt_i32 s81, 3
	s_cbranch_scc0 .LBB0_551
	s_add_i32 s0, 0, 0x20170
	s_waitcnt vmcnt(0)
	v_mov_b32_e32 v0, s0
	ds_read_b32 v2, v0
	s_cmp_eq_u32 s89, 0
	s_waitcnt vmcnt(0) lgkmcnt(0)
	s_barrier
	s_cbranch_scc1 .LBB0_506
	v_mov_b32_e32 v0, s0
	ds_read_b32 v0, v0
	s_waitcnt lgkmcnt(0)
	v_cmp_ne_u32_e32 vcc, v0, v2
	s_cbranch_vccnz .LBB0_505
	s_cmp_gt_i32 s89, 7
	s_cselect_b64 s[0:1], -1, 0
	s_lshl_b32 s2, s89, 3
	s_add_i32 s3, 0, 0x20174
	s_add_i32 s10, s2, 0
	v_add_u32_e32 v3, 1, v2
	s_mov_b32 s28, 0
	v_mov_b32_e32 v4, s3
	s_add_i32 s2, s10, 0x20180
	v_mov_b32_e32 v1, 0
	s_mov_b32 s3, 0x10000
	v_mov_b32_e32 v5, 0x10001
	s_add_i32 s10, s10, 0x20184
	s_movk_i32 s11, 0x4000
	s_mov_b32 s12, 0x8000
	s_mov_b32 s13, 0xc000
	s_mov_b32 s14, 0x14000
	s_mov_b32 s15, 0x18000
	s_mov_b32 s16, 0x1c000
	s_mov_b32 s17, 0x20000
	s_mov_b32 s18, 0x24000
	s_mov_b32 s19, 0x28000
	s_mov_b32 s20, 0x2c000
	s_mov_b32 s21, 0x30000
	s_mov_b32 s22, 0x34000
	s_mov_b32 s23, 0x38000
	s_mov_b32 s24, 0x3c000
	s_mov_b32 s25, 0xc3e00000
	s_movk_i32 s26, 0x1000
	s_add_i32 s27, 0, 0x20170
	v_mov_b32_e32 v6, 0x43e00000
	s_branch .LBB0_484

; #define BOTH(k) (IN(k) && IN((k) + 1))
; #define GRID_BAR_CV() xcd_barrier_cv(bar, cvw)
; __device__ __forceinline__ void xcd_barrier_cv(const XcdBarrier& b, const CvWork& w) {
;     asm volatile("s_waitcnt vmcnt(0)" ::: "memory");
;     const unsigned g0 = w.rel[0];
;     __syncthreads();
;     if (b.wave == 0) {
;         xb_wave0(b, w.rel + 1, g0 + 1u);
;         w.rel[0] = g0 + 1u;
;     } else if (b.wave != 0) {
;         unsigned guard = 0;
;         while (w.rel[0] == g0) { if (w.rel[1] == g0 + 1u || b.wave > 4) { __builtin_amdgcn_s_sleep(1); continue; }
;             if (!cv_one(w)) __builtin_amdgcn_s_sleep(4); if (++guard > (1u << 22)) break; }
; __global__ void __launch_bounds__(NTHR, 2) fwd(Args args) {
;     ...
;         if (BOTH(3)) GRID_BAR_CV();
.LBB0_643:
	s_cmp_lt_i32 s81, 5
	s_cbranch_scc1 .LBB0_715
	s_add_i32 s0, 0, 0x20170
	s_waitcnt vmcnt(0)
	v_mov_b32_e32 v0, s0
	ds_read_b32 v2, v0
	s_cmp_eq_u32 s89, 0
	s_waitcnt vmcnt(0) lgkmcnt(0)
	s_barrier
	s_cbranch_scc1 .LBB0_670
	v_mov_b32_e32 v0, s0
	ds_read_b32 v0, v0
	s_waitcnt lgkmcnt(0)
	v_cmp_ne_u32_e32 vcc, v0, v2
	s_cbranch_vccnz .LBB0_669
	s_cmp_gt_i32 s89, 7
	s_cselect_b64 s[0:1], -1, 0
	s_lshl_b32 s2, s89, 3
	s_add_i32 s3, 0, 0x20174
	s_add_i32 s10, s2, 0
	v_add_u32_e32 v3, 1, v2
	s_mov_b32 s28, 0
	v_mov_b32_e32 v4, s3
	s_add_i32 s2, s10, 0x20180
	v_mov_b32_e32 v1, 0
	s_mov_b32 s3, 0x10000
	v_mov_b32_e32 v5, 0x10001
	s_add_i32 s10, s10, 0x20184
	s_movk_i32 s11, 0x4000
	s_mov_b32 s12, 0x8000
	s_mov_b32 s13, 0xc000
	s_mov_b32 s14, 0x14000
	s_mov_b32 s15, 0x18000
	s_mov_b32 s16, 0x1c000
	s_mov_b32 s17, 0x20000
	s_mov_b32 s18, 0x24000
	s_mov_b32 s19, 0x28000
	s_mov_b32 s20, 0x2c000
	s_mov_b32 s21, 0x30000
	s_mov_b32 s22, 0x34000
	s_mov_b32 s23, 0x38000
	s_mov_b32 s24, 0x3c000
	s_mov_b32 s25, 0xc3e00000
	s_movk_i32 s26, 0x1000
	s_add_i32 s27, 0, 0x20170
	v_mov_b32_e32 v6, 0x43e00000
	s_branch .LBB0_648

; #define BOTH(k) (IN(k) && IN((k) + 1))
; #define GRID_BAR_CV() xcd_barrier_cv(bar, cvw)
; __device__ __forceinline__ void xcd_barrier_cv(const XcdBarrier& b, const CvWork& w) {
;     asm volatile("s_waitcnt vmcnt(0)" ::: "memory");
;     const unsigned g0 = w.rel[0];
;     __syncthreads();
;     if (b.wave == 0) {
;         xb_wave0(b, w.rel + 1, g0 + 1u);
;         w.rel[0] = g0 + 1u;
;     } else if (b.wave != 0) {
;         unsigned guard = 0;
;         while (w.rel[0] == g0) { if (w.rel[1] == g0 + 1u || b.wave > 4) { __builtin_amdgcn_s_sleep(1); continue; }
;             if (!cv_one(w)) __builtin_amdgcn_s_sleep(4); if (++guard > (1u << 22)) break; }
; __global__ void __launch_bounds__(NTHR, 2) fwd(Args args) {
;     ...
;         if (BOTH(4)) GRID_BAR_CV();
.LBB0_896:
	s_cmp_lt_i32 s81, 6
	s_cbranch_scc1 .LBB0_968
	s_add_i32 s0, 0, 0x20170
	s_waitcnt vmcnt(0)
	v_mov_b32_e32 v0, s0
	ds_read_b32 v2, v0
	s_cmp_eq_u32 s89, 0
	s_waitcnt vmcnt(0) lgkmcnt(0)
	s_barrier
	s_cbranch_scc1 .LBB0_923
	v_mov_b32_e32 v0, s0
	ds_read_b32 v0, v0
	s_waitcnt lgkmcnt(0)
	v_cmp_ne_u32_e32 vcc, v0, v2
	s_cbranch_vccnz .LBB0_922
	s_cmp_gt_i32 s89, 7
	s_cselect_b64 s[0:1], -1, 0
	s_lshl_b32 s2, s89, 3
	s_add_i32 s3, 0, 0x20174
	s_add_i32 s10, s2, 0
	v_add_u32_e32 v3, 1, v2
	s_mov_b32 s28, 0
	v_mov_b32_e32 v4, s3
	s_add_i32 s2, s10, 0x20180
	v_mov_b32_e32 v1, 0
	s_mov_b32 s3, 0x10000
	v_mov_b32_e32 v5, 0x10001
	s_add_i32 s10, s10, 0x20184
	s_movk_i32 s11, 0x4000
	s_mov_b32 s12, 0x8000
	s_mov_b32 s13, 0xc000
	s_mov_b32 s14, 0x14000
	s_mov_b32 s15, 0x18000
	s_mov_b32 s16, 0x1c000
	s_mov_b32 s17, 0x20000
	s_mov_b32 s18, 0x24000
	s_mov_b32 s19, 0x28000
	s_mov_b32 s20, 0x2c000
	s_mov_b32 s21, 0x30000
	s_mov_b32 s22, 0x34000
	s_mov_b32 s23, 0x38000
	s_mov_b32 s24, 0x3c000
	s_mov_b32 s25, 0xc3e00000
	s_movk_i32 s26, 0x1000
	s_add_i32 s27, 0, 0x20170
	v_mov_b32_e32 v6, 0x43e00000
	s_branch .LBB0_901

; #define BOTH(k) (IN(k) && IN((k) + 1))
; #define GRID_BAR_CV() xcd_barrier_cv(bar, cvw)
; __device__ __forceinline__ void xcd_barrier_cv(const XcdBarrier& b, const CvWork& w) {
;     asm volatile("s_waitcnt vmcnt(0)" ::: "memory");
;     const unsigned g0 = w.rel[0];
;     __syncthreads();
;     if (b.wave == 0) {
;         xb_wave0(b, w.rel + 1, g0 + 1u);
;         w.rel[0] = g0 + 1u;
;     } else if (b.wave != 0) {
;         unsigned guard = 0;
;         while (w.rel[0] == g0) { if (w.rel[1] == g0 + 1u || b.wave > 4) { __builtin_amdgcn_s_sleep(1); continue; }
;             if (!cv_one(w)) __builtin_amdgcn_s_sleep(4); if (++guard > (1u << 22)) break; }
; __global__ void __launch_bounds__(NTHR, 2) fwd(Args args) {
;     ...
;         if (BOTH(5)) GRID_BAR_CV();
.LBB0_972:
	s_cmp_lt_u32 s81, 7
	s_cbranch_scc1 .LBB0_1044
	s_add_i32 s0, 0, 0x20170
	s_waitcnt vmcnt(0)
	v_mov_b32_e32 v0, s0
	ds_read_b32 v2, v0
	s_cmp_eq_u32 s89, 0
	s_waitcnt lgkmcnt(0)
	s_barrier
	s_cbranch_scc1 .LBB0_999
	v_mov_b32_e32 v0, s0
	ds_read_b32 v0, v0
	s_waitcnt lgkmcnt(0)
	v_cmp_ne_u32_e32 vcc, v0, v2
	s_cbranch_vccnz .LBB0_998
	s_cmp_gt_i32 s89, 7
	s_cselect_b64 s[0:1], -1, 0
	s_lshl_b32 s2, s89, 3
	s_add_i32 s3, 0, 0x20174
	s_add_i32 s10, s2, 0
	v_add_u32_e32 v3, 1, v2
	s_mov_b32 s28, 0
	v_mov_b32_e32 v4, s3
	s_add_i32 s2, s10, 0x20180
	v_mov_b32_e32 v1, 0
	s_mov_b32 s3, 0x10000
	v_mov_b32_e32 v5, 0x10001
	s_add_i32 s10, s10, 0x20184
	s_movk_i32 s11, 0x4000
	s_mov_b32 s12, 0x8000
	s_mov_b32 s13, 0xc000
	s_mov_b32 s14, 0x14000
	s_mov_b32 s15, 0x18000
	s_mov_b32 s16, 0x1c000
	s_mov_b32 s17, 0x20000
	s_mov_b32 s18, 0x24000
	s_mov_b32 s19, 0x28000
	s_mov_b32 s20, 0x2c000
	s_mov_b32 s21, 0x30000
	s_mov_b32 s22, 0x34000
	s_mov_b32 s23, 0x38000
	s_mov_b32 s24, 0x3c000
	s_mov_b32 s25, 0xc3e00000
	s_movk_i32 s26, 0x1000
	s_add_i32 s27, 0, 0x20170
	v_mov_b32_e32 v6, 0x43e00000
	s_branch .LBB0_977

; #define BOTH(k) (IN(k) && IN((k) + 1))
; #define GRID_BAR_CV() xcd_barrier_cv(bar, cvw)
; __device__ __forceinline__ void xcd_barrier_cv(const XcdBarrier& b, const CvWork& w) {
;     asm volatile("s_waitcnt vmcnt(0)" ::: "memory");
;     const unsigned g0 = w.rel[0];
;     __syncthreads();
;     if (b.wave == 0) {
;         xb_wave0(b, w.rel + 1, g0 + 1u);
;         w.rel[0] = g0 + 1u;
;     } else if (b.wave != 0) {
;         unsigned guard = 0;
;         while (w.rel[0] == g0) { if (w.rel[1] == g0 + 1u || b.wave > 4) { __builtin_amdgcn_s_sleep(1); continue; }
;             if (!cv_one(w)) __builtin_amdgcn_s_sleep(4); if (++guard > (1u << 22)) break; }
; __global__ void __launch_bounds__(NTHR, 2) fwd(Args args) {
;     ...
;         if (BOTH(6)) GRID_BAR_CV();
.LBB0_1090:
	s_add_i32 s0, 0, 0x20170
	s_waitcnt vmcnt(0)
	v_mov_b32_e32 v0, s0
	ds_read_b32 v2, v0
	s_cmp_eq_u32 s89, 0
	s_waitcnt lgkmcnt(0)
	s_barrier
	s_cbranch_scc1 .LBB0_1116
	v_mov_b32_e32 v0, s0
	ds_read_b32 v0, v0
	s_waitcnt lgkmcnt(0)
	v_cmp_ne_u32_e32 vcc, v0, v2
	s_cbranch_vccnz .LBB0_1115
	s_cmp_gt_i32 s89, 7
	s_cselect_b64 s[0:1], -1, 0
	s_lshl_b32 s2, s89, 3
	s_add_i32 s3, 0, 0x20174
	s_add_i32 s10, s2, 0
	v_add_u32_e32 v3, 1, v2
	s_mov_b32 s28, 0
	v_mov_b32_e32 v4, s3
	s_add_i32 s2, s10, 0x20180
	v_mov_b32_e32 v1, 0
	s_mov_b32 s3, 0x10000
	v_mov_b32_e32 v5, 0x10001
	s_add_i32 s10, s10, 0x20184
	s_movk_i32 s11, 0x4000
	s_mov_b32 s12, 0x8000
	s_mov_b32 s13, 0xc000
	s_mov_b32 s14, 0x14000
	s_mov_b32 s15, 0x18000
	s_mov_b32 s16, 0x1c000
	s_mov_b32 s17, 0x20000
	s_mov_b32 s18, 0x24000
	s_mov_b32 s19, 0x28000
	s_mov_b32 s20, 0x2c000
	s_mov_b32 s21, 0x30000
	s_mov_b32 s22, 0x34000
	s_mov_b32 s23, 0x38000
	s_mov_b32 s24, 0x3c000
	s_mov_b32 s25, 0xc3e00000
	s_movk_i32 s26, 0x1000
	s_add_i32 s27, 0, 0x20170
	v_mov_b32_e32 v6, 0x43e00000
	s_branch .LBB0_1094

; #define BOTH(k) (IN(k) && IN((k) + 1))
; #define GRID_BAR_CV() xcd_barrier_cv(bar, cvw)
; __device__ __forceinline__ void xcd_barrier_cv(const XcdBarrier& b, const CvWork& w) {
;     asm volatile("s_waitcnt vmcnt(0)" ::: "memory");
;     const unsigned g0 = w.rel[0];
;     __syncthreads();
;     if (b.wave == 0) {
;         xb_wave0(b, w.rel + 1, g0 + 1u);
;         w.rel[0] = g0 + 1u;
;     } else if (b.wave != 0) {
;         unsigned guard = 0;
;         while (w.rel[0] == g0) { if (w.rel[1] == g0 + 1u || b.wave > 4) { __builtin_amdgcn_s_sleep(1); continue; }
;             if (!cv_one(w)) __builtin_amdgcn_s_sleep(4); if (++guard > (1u << 22)) break; }
; __global__ void __launch_bounds__(NTHR, 2) fwd(Args args) {
;     ...
;         if (BOTH(7)) GRID_BAR_CV();
.LBB0_1217:
	s_cmp_lt_i32 s81, 9
	s_cbranch_scc1 .LBB0_1289
	s_add_i32 s0, 0, 0x20170
	s_waitcnt vmcnt(0)
	v_mov_b32_e32 v0, s0
	ds_read_b32 v2, v0
	s_cmp_eq_u32 s89, 0
	s_waitcnt vmcnt(0) lgkmcnt(0)
	s_barrier
	s_cbranch_scc1 .LBB0_1244
	v_mov_b32_e32 v0, s0
	ds_read_b32 v0, v0
	s_waitcnt lgkmcnt(0)
	v_cmp_ne_u32_e32 vcc, v0, v2
	s_cbranch_vccnz .LBB0_1243
	s_cmp_gt_i32 s89, 7
	s_cselect_b64 s[0:1], -1, 0
	s_lshl_b32 s2, s89, 3
	s_add_i32 s3, 0, 0x20174
	s_add_i32 s10, s2, 0
	v_add_u32_e32 v3, 1, v2
	s_mov_b32 s28, 0
	v_mov_b32_e32 v4, s3
	s_add_i32 s2, s10, 0x20180
	v_mov_b32_e32 v1, 0
	s_mov_b32 s3, 0x10000
	v_mov_b32_e32 v5, 0x10001
	s_add_i32 s10, s10, 0x20184
	s_movk_i32 s11, 0x4000
	s_mov_b32 s12, 0x8000
	s_mov_b32 s13, 0xc000
	s_mov_b32 s14, 0x14000
	s_mov_b32 s15, 0x18000
	s_mov_b32 s16, 0x1c000
	s_mov_b32 s17, 0x20000
	s_mov_b32 s18, 0x24000
	s_mov_b32 s19, 0x28000
	s_mov_b32 s20, 0x2c000
	s_mov_b32 s21, 0x30000
	s_mov_b32 s22, 0x34000
	s_mov_b32 s23, 0x38000
	s_mov_b32 s24, 0x3c000
	s_mov_b32 s25, 0xc3e00000
	s_movk_i32 s26, 0x1000
	s_add_i32 s27, 0, 0x20170
	v_mov_b32_e32 v6, 0x43e00000
	s_branch .LBB0_1222

; __device__ __forceinline__ int lane_id_now() { unsigned z = 0u; asm volatile("" : "+v"(z)); return (int)__builtin_amdgcn_mbcnt_hi(~0u, __builtin_amdgcn_mbcnt_lo(~0u, z)); }
; __device__ __forceinline__ bool cv_one(const CvWork& w) {
;     if (w.wave == 0) return false;
;     int it = __builtin_amdgcn_readfirstlane(w.cur[2 * w.wave]); const int end = __builtin_amdgcn_readfirstlane(w.cur[2 * w.wave + 1]);
;     if (it >= end) {
;         if (it > CV_ITEMS) return false;
;         unsigned base = 0u; if (lane_id_now() == 0) base = __hip_atomic_fetch_add(w.q, (unsigned)CV_BATCH, __ATOMIC_RELAXED, __HIP_MEMORY_SCOPE_AGENT);
;         base = __builtin_amdgcn_readfirstlane(base);
;         if (base >= (unsigned)CV_ITEMS) { w.cur[2 * w.wave] = CV_ITEMS + 1; w.cur[2 * w.wave + 1] = 0; return false; }
;         it = (int)base; w.cur[2 * w.wave + 1] = (int)base + CV_BATCH;
;     }
.LBB0_1416:
	ds_read_b32 v0, v2
	ds_read_b32 v5, v2 offset:4
	s_waitcnt lgkmcnt(1)
	v_readfirstlane_b32 s28, v0
	s_waitcnt lgkmcnt(0)
	v_readfirstlane_b32 s4, v5
	s_cmp_lt_i32 s28, s4
	s_mov_b64 s[4:5], -1
	s_cbranch_scc1 .LBB0_1427
	s_cmp_gt_u32 s89, 5
	s_cbranch_scc1 .LBB0_1430
	s_cmp_lt_i32 s28, 0x10001
	s_mov_b64 s[6:7], 0
	s_cbranch_scc0 .LBB0_1428
	v_mov_b32_e32 v5, 0
	v_mov_b32_e32 v0, 0
	v_mbcnt_lo_u32_b32 v5, -1, v5
	v_mbcnt_hi_u32_b32 v5, -1, v5
	v_cmp_eq_u32_e32 vcc, 0, v5
	s_and_saveexec_b64 s[6:7], vcc
	s_cbranch_execz .LBB0_1422
	s_mov_b64 s[10:11], exec
	v_mbcnt_lo_u32_b32 v0, s10, 0
	v_mbcnt_hi_u32_b32 v0, s11, v0
	v_cmp_eq_u32_e32 vcc, 0, v0
	s_and_saveexec_b64 s[8:9], vcc
	s_cbranch_execz .LBB0_1421
	s_bcnt1_i32_b64 s10, s[10:11]
	s_lshl_b32 s10, s10, 2
	v_mov_b32_e32 v5, s10
	global_atomic_add v5, v1, v5, s[90:91] sc0
